# attention QK phase: counted lgkmcnt waits at each MFMA's own fragment instead of four full LDS drains
# baseline (speedup 1.0000x reference)
.LBB2_22:
	s_or_b64 exec, exec, s[44:45]
	v_cmp_ge_u32_e32 vcc, s52, v50
	s_and_saveexec_b64 s[44:45], vcc
	s_cbranch_execz .LBB2_29
	v_and_or_b32 v1, s48, 1, v100
	v_mul_u32_u24_e32 v46, 0x5000, v1
	v_or_b32_e32 v42, v46, v97
	v_add_u32_e32 v75, v42, v94
	ds_read_b128 v[34:37], v75
	v_add_u32_e32 v73, v42, v95
	ds_read_b128 v[42:45], v73
	v_sub_f32_e32 v38, 0x41000000, v69
	v_or_b32_e32 v47, v46, v96
	v_mov_b32_e32 v39, v38
	v_mov_b32_e32 v40, v38
	v_mov_b32_e32 v41, v38
	v_add_u32_e32 v48, v47, v101
	ds_read_b128 v[52:55], v48 offset:16384
	s_waitcnt lgkmcnt(2)
	v_mfma_f32_16x16x32_f16 v[34:37], v[34:37], v[6:9], v[38:41]
	v_or_b32_e32 v46, v46, v102
	v_cmp_eq_u32_e32 vcc, s52, v50
	s_waitcnt lgkmcnt(1)
	v_mfma_f32_16x16x32_f16 v[34:37], v[42:45], v[10:13], v[34:37]
	v_add_u32_e32 v42, v46, v94
	ds_read_b128 v[42:45], v42
	v_add_u32_e32 v46, v46, v95
	s_waitcnt lgkmcnt(1)
	v_mfma_f32_16x16x32_f16 v[56:59], v[52:55], v[2:5], 0
	ds_read_b128 v[52:55], v46
	v_add_u32_e32 v46, v47, v103
	ds_read_b128 v[60:63], v46 offset:16384
	s_waitcnt lgkmcnt(2)
	v_mfma_f32_16x16x32_f16 v[42:45], v[42:45], v[6:9], v[38:41]
	v_mad_u32_u24 v46, v1, s50, v104
	v_add_u32_e32 v48, v46, v94
	ds_read_b128 v[110:113], v48
	s_waitcnt lgkmcnt(2)
	v_mfma_f32_16x16x32_f16 v[42:45], v[52:55], v[10:13], v[42:45]
	v_add_u32_e32 v46, v46, v95
	v_fma_f32 v34, |v56|, s64, v34
	v_fma_f32 v36, |v58|, s64, v36
	s_waitcnt lgkmcnt(1)
	v_mfma_f32_16x16x32_f16 v[52:55], v[60:63], v[2:5], 0
	ds_read_b128 v[60:63], v46
	v_add_u32_e32 v46, v47, v105
	ds_read_b128 v[114:117], v46 offset:16384
	s_waitcnt lgkmcnt(2)
	v_mfma_f32_16x16x32_f16 v[110:113], v[110:113], v[6:9], v[38:41]
	v_mad_u32_u24 v46, v1, s50, v106
	v_add_u32_e32 v1, v46, v94
	s_waitcnt lgkmcnt(1)
	v_mfma_f32_16x16x32_f16 v[60:63], v[60:63], v[10:13], v[110:113]
	s_nop 4
	ds_read_b128 v[110:113], v1
	v_fma_f32 v1, |v57|, s64, v35
	v_add_u32_e32 v35, v46, v95
	ds_read_b128 v[122:125], v35
	v_add_u32_e32 v35, v47, v107
	s_waitcnt lgkmcnt(2)
	v_mfma_f32_16x16x32_f16 v[118:121], v[114:117], v[2:5], 0
	ds_read_b128 v[114:117], v35 offset:16384
	v_fma_f32 v35, |v59|, s64, v37
	v_fma_f32 v37, |v53|, s64, v43
	s_waitcnt lgkmcnt(2)
	v_mfma_f32_16x16x32_f16 v[110:113], v[110:113], v[6:9], v[38:41]
	s_waitcnt lgkmcnt(1)
	v_mfma_f32_16x16x32_f16 v[56:59], v[122:125], v[10:13], v[110:113]
	s_nop 1
	v_fma_f32 v38, |v52|, s64, v42
	v_fma_f32 v40, |v54|, s64, v44
	v_fma_f32 v39, |v55|, s64, v45
	s_waitcnt lgkmcnt(0)
	v_mfma_f32_16x16x32_f16 v[52:55], v[114:117], v[2:5], 0
	v_fma_f32 v42, |v118|, s64, v60
	v_fma_f32 v41, |v119|, s64, v61
	v_fma_f32 v44, |v120|, s64, v62
	v_fma_f32 v43, |v121|, s64, v63
	s_nop 6
	v_fma_f32 v46, |v52|, s64, v56
	v_fma_f32 v45, |v53|, s64, v57
	v_fma_f32 v48, |v54|, s64, v58
	v_fma_f32 v47, |v55|, s64, v59
	s_and_saveexec_b64 s[46:47], vcc
	s_cbranch_execz .LBB2_25
	v_mov_b32_e32 v50, s51
	v_cndmask_b32_e64 v50, v34, v50, s[36:37]
	v_cndmask_b32_e64 v34, v50, v34, s[4:5]
	v_mov_b32_e32 v50, s51
	v_cndmask_b32_e64 v1, v108, v1, s[4:5]
	v_cndmask_b32_e64 v36, v36, v108, s[6:7]
	v_cndmask_b32_e64 v35, v35, v108, s[8:9]
	v_cndmask_b32_e64 v38, v38, v50, s[10:11]
	v_cndmask_b32_e64 v37, v37, v108, s[12:13]
	v_cndmask_b32_e64 v40, v40, v108, s[14:15]
	v_cndmask_b32_e64 v39, v39, v108, s[16:17]
	v_cndmask_b32_e64 v42, v42, v50, s[18:19]
	v_cndmask_b32_e64 v41, v41, v108, s[20:21]
	v_cndmask_b32_e64 v44, v44, v108, s[22:23]
	v_cndmask_b32_e64 v43, v43, v108, s[24:25]
	v_cndmask_b32_e64 v46, v46, v50, s[26:27]
	v_cndmask_b32_e64 v45, v45, v108, s[28:29]
	v_cndmask_b32_e64 v48, v48, v108, s[30:31]
	v_cndmask_b32_e64 v47, v47, v108, s[34:35]
